# routing norm: router staging loads issued at phase start so their latency overlaps the shift/scale fill
# speedup vs baseline: 1.0103x; 1.0059x over previous
.LBB0_2053:
	s_or_b64 exec, exec, s[4:5]
	v_readlane_b32 s0, v254, 18
	v_readlane_b32 s1, v254, 19
	s_waitcnt lgkmcnt(0)
	s_barrier
	s_load_dwordx4 s[16:19], s[0:1], 0x150
	s_load_dwordx2 s[8:9], s[0:1], 0x188
	v_mov_b32_e32 v0, s2
	v_mbcnt_lo_u32_b32 v8, -1, 0
	v_mbcnt_hi_u32_b32 v8, -1, v8
	v_readlane_b32 s0, v254, 0
	v_readfirstlane_b32 s24, v0
	v_mov_b32_e32 v0, 0
	v_add_u32_e32 v2, s0, v8
	v_readfirstlane_b32 s25, v0
	s_ashr_i32 s27, s25, 31
	s_waitcnt lgkmcnt(0)
	v_lshlrev_b32_e32 v236, 4, v2
	global_load_dwordx4 v[204:207], v236, s[18:19]
	v_add_u32_e32 v237, 0x2000, v236
	global_load_dwordx4 v[208:211], v237, s[18:19]
	v_add_u32_e32 v237, 0x4000, v236
	global_load_dwordx4 v[212:215], v237, s[18:19]
	v_add_u32_e32 v237, 0x6000, v236
	global_load_dwordx4 v[216:219], v237, s[18:19]
	v_add_u32_e32 v237, 0x8000, v236
	global_load_dwordx4 v[220:223], v237, s[18:19]
	v_add_u32_e32 v237, 0xa000, v236
	global_load_dwordx4 v[224:227], v237, s[18:19]
	v_add_u32_e32 v237, 0xc000, v236
	global_load_dwordx4 v[228:231], v237, s[18:19]
	v_add_u32_e32 v237, 0xe000, v236
	global_load_dwordx4 v[232:235], v237, s[18:19]
	s_add_u32 s22, s8, s25
	s_movk_i32 s26, 0x1000
	v_mov_b32_e32 v1, 0
	s_addc_u32 s23, s9, s27
	v_cmp_gt_i32_e32 vcc, s26, v2
	s_and_saveexec_b64 s[4:5], vcc
	s_cbranch_execz .LBB0_2066
	s_ashr_i32 s0, s24, 31
	s_lshr_b32 s0, s0, 26
	v_max_i32_e32 v0, 0xe00, v2
	s_add_i32 s0, s24, s0
	v_sub_u32_e32 v0, v0, v2
	s_ashr_i32 s28, s0, 6
	s_movk_i32 s0, 0x1ff
	v_add_u32_e32 v0, 0x1ff, v0
	v_cmp_lt_u32_e32 vcc, s0, v0
	s_mov_b64 s[12:13], -1
	s_and_saveexec_b64 s[10:11], vcc
	s_cbranch_execz .LBB0_2063
	s_add_i32 s0, s28, 4
	s_mul_hi_i32 s1, s0, 0xc000
	s_mul_i32 s0, s0, 0xc000
	v_lshrrev_b32_e32 v0, 9, v0
	s_add_u32 s0, s22, s0
	s_addc_u32 s1, s23, s1
	v_add_u32_e32 v4, -1, v0
	s_add_u32 s12, s0, 0x406000
	v_add_u32_e32 v3, 0x200, v2
	v_lshrrev_b32_e32 v5, 1, v4
	s_addc_u32 s13, s1, 0
	v_add_u32_e32 v6, 1, v5
	v_cmp_lt_u32_e32 vcc, 13, v4
	v_mov_b32_e32 v10, 0
	v_mov_b64_e32 v[4:5], v[2:3]
	s_and_saveexec_b64 s[14:15], vcc
	s_cbranch_execz .LBB0_2059
	s_lshl_b32 s0, s76, 8
	s_add_i32 s0, s0, 0
	v_and_b32_e32 v7, -8, v6
	s_mov_b32 s29, 0
	v_lshl_add_u32 v9, v8, 2, s0
	s_mov_b64 s[20:21], 0
	v_mov_b64_e32 v[4:5], v[2:3]

.LBB0_2066:
	s_or_b64 exec, exec, s[4:5]
	s_lshl_b32 s27, s24, 5
	s_add_i32 s27, s27, s76
	s_add_u32 s29, s22, 0x3df80000
	s_addc_u32 s30, s23, 0
	s_add_u32 s14, s22, 0x8000
	s_addc_u32 s15, s23, 0
	s_add_u32 s31, s22, 0x460000
	s_addc_u32 s33, s23, 0
	s_add_u32 s35, s22, 0x470000
	v_ashrrev_i32_e32 v9, 31, v8
	s_addc_u32 s36, s23, 0
	v_lshlrev_b64 v[2:3], 4, v[8:9]
	s_add_u32 s37, s22, 0x480000
	v_lshl_add_u64 v[22:23], s[6:7], 0, v[2:3]
	s_addc_u32 s38, s23, 0
	v_readlane_b32 s0, v254, 9
	v_readlane_b32 s6, v254, 45
	v_readlane_b32 s1, v254, 10
	s_add_u32 s0, s0, s6
	v_readlane_b32 s6, v254, 46
	s_addc_u32 s1, s1, s6
	v_lshl_add_u64 v[2:3], s[0:1], 0, v[2:3]
	s_mov_b64 s[0:1], 0x2bc80400
	v_lshl_add_u64 v[24:25], v[2:3], 0, s[0:1]
	v_mov_b32_e32 v2, v1
	v_mov_b32_e32 v3, v1
	v_mov_b32_e32 v4, v1
	v_mov_b32_e32 v5, v1
	v_mov_b32_e32 v6, v1
	v_mov_b32_e32 v7, v1
	v_lshlrev_b32_e32 v46, 2, v8
	v_cmp_eq_u32_e64 s[4:5], 0, v8
	v_lshl_add_u32 v49, v8, 4, 0
	v_mov_b32_e32 v0, v1
	v_lshlrev_b64 v[26:27], 2, v[8:9]
	v_mov_b64_e32 v[8:9], v[6:7]
	v_xor_b32_e32 v47, 64, v46
	v_xor_b32_e32 v48, 0x80, v46
	s_mov_b32 s28, 0
	v_mov_b32_e32 v50, 0x358637bd
	s_mov_b32 s39, 0xf800000
	v_mov_b32_e32 v51, 0x260
	s_mov_b32 s40, 0xc3e00000
	s_mov_b64 s[20:21], 0x800
	v_mov_b32_e32 v52, 0x43e00000
	v_mov_b32_e32 v53, 1
	s_mov_b32 s22, s27
	v_mov_b64_e32 v[6:7], v[4:5]
	v_mov_b64_e32 v[4:5], v[2:3]
	v_mov_b64_e32 v[2:3], v[0:1]
	v_lshrrev_b32_e32 v200, 2, v46
	v_lshl_add_u32 v200, s76, 6, v200
	v_and_b32_e32 v202, 7, v200
	v_lshrrev_b32_e32 v203, 3, v200
	v_mul_u32_u24_e32 v202, 0x2020, v202
	v_lshl_add_u32 v203, v203, 4, v202
	v_add_u32_e32 v150, 0x4000, v49
	s_waitcnt vmcnt(0)
	ds_write_b128 v203, v[204:207] offset:16384
	ds_write_b128 v203, v[208:211] offset:17408
	ds_write_b128 v203, v[212:215] offset:18432
	ds_write_b128 v203, v[216:219] offset:19456
	ds_write_b128 v203, v[220:223] offset:20480
	ds_write_b128 v203, v[224:227] offset:21504
	ds_write_b128 v203, v[228:231] offset:22528
	ds_write_b128 v203, v[232:235] offset:23552
	s_waitcnt lgkmcnt(0)
	s_barrier
	v_add_u32_e32 v152, 0x1000, v49
	global_load_dwordx4 v[188:191], v49, s[16:17]
	global_load_dwordx4 v[192:195], v49, s[16:17] offset:1024
	global_load_dwordx4 v[196:199], v49, s[16:17] offset:2048
	global_load_dwordx4 v[200:203], v49, s[16:17] offset:3072
	global_load_dwordx4 v[204:207], v152, s[16:17]
	global_load_dwordx4 v[208:211], v152, s[16:17] offset:1024
	global_load_dwordx4 v[212:215], v152, s[16:17] offset:2048
	global_load_dwordx4 v[216:219], v152, s[16:17] offset:3072
	s_branch .LBB0_2068
